# rwkv_chunk_pre unit->wave map changed so every workgroup has 4 waves with 9 units and 4 with 8 (one of each per SIMD) instead of whole workgroups with 9
# speedup vs baseline: 1.0124x; 1.0033x over previous
.LBB0_635:
	v_readlane_b32 s2, v251, 14
	v_readlane_b32 s3, v251, 15
	s_cmp_le_i32 s2, s10
	s_cselect_b64 s[0:1], -1, 0
	s_cmp_lt_i32 s10, s3
	s_cselect_b64 s[2:3], -1, 0
	s_and_b64 s[0:1], s[0:1], s[2:3]
	s_andn2_b64 vcc, exec, s[0:1]
	s_cbranch_vccnz .LBB0_753
	v_mov_b32_e32 v46, v0
	s_nop 0
	v_readfirstlane_b32 s0, v46
	s_ashr_i32 s4, s0, 6
	v_and_b32_e32 v48, 63, v46
	v_writelane_b32 v254, s0, 39
	v_readlane_b32 s0, v251, 10
	s_waitcnt lgkmcnt(0)
	s_add_i32 s95, s4, s0
	s_lshr_b32 s100, s4, 2
	s_lshl_b32 s100, s100, 10
	s_and_b32 s101, s4, 3
	s_add_u32 s100, s100, s101
	s_lshr_b32 s101, s0, 1
	s_add_u32 s95, s100, s101
	v_readlane_b32 s0, v251, 11
	v_readlane_b32 s1, v251, 12
	s_cmpk_lt_i32 s95, 0x4400
	v_lshrrev_b32_e32 v49, 4, v48
	s_waitcnt lgkmcnt(0)
	v_mov_b64_e32 v[2:3], s[0:1]
	s_waitcnt vmcnt(0) lgkmcnt(0)
	flat_load_dwordx2 v[4:5], v[2:3] offset:96 sc0 sc1
	s_waitcnt vmcnt(0) lgkmcnt(0)
	v_readfirstlane_b32 s2, v5
	v_readfirstlane_b32 s3, v4
	flat_load_dwordx2 v[4:5], v[2:3] offset:104 sc0 sc1
	s_waitcnt vmcnt(0) lgkmcnt(0)
	v_readfirstlane_b32 s93, v5
	v_readfirstlane_b32 s92, v4
	s_waitcnt vmcnt(0) lgkmcnt(0)
	flat_load_dwordx2 v[4:5], v[2:3] offset:120 sc0 sc1
	s_waitcnt vmcnt(0) lgkmcnt(0)
	v_readfirstlane_b32 s7, v5
	v_readfirstlane_b32 s6, v4
	s_waitcnt vmcnt(0) lgkmcnt(0)
	flat_load_dwordx2 v[4:5], v[2:3] offset:144 sc0 sc1
	s_waitcnt vmcnt(0) lgkmcnt(0)
	v_readfirstlane_b32 s39, v5
	v_readfirstlane_b32 s38, v4
	flat_load_dwordx2 v[4:5], v[2:3] offset:152 sc0 sc1
	s_waitcnt vmcnt(0) lgkmcnt(0)
	v_readfirstlane_b32 s85, v5
	v_readfirstlane_b32 s84, v4
	flat_load_dwordx2 v[4:5], v[2:3] offset:160 sc0 sc1
	s_waitcnt vmcnt(0) lgkmcnt(0)
	v_readfirstlane_b32 s13, v5
	v_readfirstlane_b32 s12, v4
	s_waitcnt vmcnt(0) lgkmcnt(0)
	flat_load_dwordx2 v[4:5], v[2:3] offset:184 sc0 sc1
	s_waitcnt vmcnt(0) lgkmcnt(0)
	v_readfirstlane_b32 s0, v5
	s_nop 1
	v_writelane_b32 v254, s0, 40
	v_readfirstlane_b32 s0, v4
	flat_load_dwordx2 v[4:5], v[2:3] offset:192 sc0 sc1
	s_waitcnt vmcnt(0)
	v_writelane_b32 v254, s0, 41
	s_waitcnt lgkmcnt(0)
	v_readfirstlane_b32 s0, v5
	s_nop 1
	v_writelane_b32 v254, s0, 42
	v_readfirstlane_b32 s0, v4
	flat_load_dwordx2 v[4:5], v[2:3] offset:200 sc0 sc1
	s_waitcnt vmcnt(0)
	v_writelane_b32 v254, s0, 43
	s_waitcnt lgkmcnt(0)
	v_readfirstlane_b32 s0, v5
	s_nop 1
	v_writelane_b32 v254, s0, 44
	v_readfirstlane_b32 s0, v4
	s_waitcnt vmcnt(0) lgkmcnt(0)
	flat_load_dwordx2 v[4:5], v[2:3] offset:256 sc0 sc1
	s_waitcnt vmcnt(0)
	flat_load_dwordx2 v[2:3], v[2:3] offset:264 sc0 sc1
	s_waitcnt vmcnt(0)
	v_writelane_b32 v254, s0, 45
	s_cbranch_scc1 .LBB0_638
	s_waitcnt lgkmcnt(0)
	v_lshrrev_b32_e32 v2, 4, v48
	s_lshl_b32 s94, s50, 9
	v_lshlrev_b32_e32 v50, 3, v2
	s_mov_b64 s[0:1], 0
	s_branch .LBB0_639

	.amdhsa_kernel _Z6mk_fwd4Args
		.amdhsa_group_segment_fixed_size 0
		.amdhsa_private_segment_fixed_size 0
		.amdhsa_kernarg_size 552
		.amdhsa_user_sgpr_count 2
		.amdhsa_user_sgpr_dispatch_ptr 0
		.amdhsa_user_sgpr_queue_ptr 0
		.amdhsa_user_sgpr_kernarg_segment_ptr 1
		.amdhsa_user_sgpr_dispatch_id 0
		.amdhsa_user_sgpr_kernarg_preload_length 0
		.amdhsa_user_sgpr_kernarg_preload_offset 0
		.amdhsa_user_sgpr_private_segment_size 0
		.amdhsa_uses_dynamic_stack 0
		.amdhsa_enable_private_segment 0
		.amdhsa_system_sgpr_workgroup_id_x 1
		.amdhsa_system_sgpr_workgroup_id_y 0
		.amdhsa_system_sgpr_workgroup_id_z 0
		.amdhsa_system_sgpr_workgroup_info 0
		.amdhsa_system_vgpr_workitem_id 0
		.amdhsa_next_free_vgpr 255
		.amdhsa_next_free_sgpr 102
		.amdhsa_accum_offset 256
		.amdhsa_reserve_vcc 1
		.amdhsa_float_round_mode_32 0
		.amdhsa_float_round_mode_16_64 0
		.amdhsa_float_denorm_mode_32 3
		.amdhsa_float_denorm_mode_16_64 3
		.amdhsa_dx10_clamp 1
		.amdhsa_ieee_mode 1
		.amdhsa_fp16_overflow 0
		.amdhsa_tg_split 0
		.amdhsa_exception_fp_ieee_invalid_op 0
		.amdhsa_exception_fp_denorm_src 0
		.amdhsa_exception_fp_ieee_div_zero 0
		.amdhsa_exception_fp_ieee_overflow 0
		.amdhsa_exception_fp_ieee_underflow 0
		.amdhsa_exception_fp_ieee_inexact 0
		.amdhsa_exception_int_div_zero 0
	.end_amdhsa_kernel

amdhsa.kernels:
  - .agpr_count:     0
    .args:
      - .offset:         0
        .size:           296
        .value_kind:     by_value
      - .offset:         296
        .size:           4
        .value_kind:     hidden_block_count_x
      - .offset:         300
        .size:           4
        .value_kind:     hidden_block_count_y
      - .offset:         304
        .size:           4
        .value_kind:     hidden_block_count_z
      - .offset:         308
        .size:           2
        .value_kind:     hidden_group_size_x
      - .offset:         310
        .size:           2
        .value_kind:     hidden_group_size_y
      - .offset:         312
        .size:           2
        .value_kind:     hidden_group_size_z
      - .offset:         314
        .size:           2
        .value_kind:     hidden_remainder_x
      - .offset:         316
        .size:           2
        .value_kind:     hidden_remainder_y
      - .offset:         318
        .size:           2
        .value_kind:     hidden_remainder_z
      - .offset:         336
        .size:           8
        .value_kind:     hidden_global_offset_x
      - .offset:         344
        .size:           8
        .value_kind:     hidden_global_offset_y
      - .offset:         352
        .size:           8
        .value_kind:     hidden_global_offset_z
      - .offset:         360
        .size:           2
        .value_kind:     hidden_grid_dims
      - .offset:         416
        .size:           4
        .value_kind:     hidden_dynamic_lds_size
    .group_segment_fixed_size: 0
    .kernarg_segment_align: 8
    .kernarg_segment_size: 552
    .language:       OpenCL C
    .language_version:
      - 2
      - 0
    .max_flat_workgroup_size: 512
    .name:           _Z6mk_fwd4Args
    .private_segment_fixed_size: 0
    .sgpr_count:     108
    .sgpr_spill_count: 341
    .symbol:         _Z6mk_fwd4Args.kd
    .uniform_work_group_size: 1
    .uses_dynamic_stack: false
    .vgpr_count:     255
    .vgpr_spill_count: 0
    .wavefront_size: 64
